# gate unit: k-mean table staged with all loads in flight and written to LDS under the query-row loads (was a load/wait loop); plus kmean-phase load de-serialisation, barrier early-invalidate, MoBA QK p
# speedup vs baseline: 1.0056x; 1.0056x over previous
.LBB0_475:
	s_mul_hi_i32 s0, s7, 0x2aaaaaab
	s_lshr_b32 s1, s0, 31
	s_lshr_b32 s0, s0, 1
	s_add_i32 s0, s0, s1
	s_mul_i32 s0, s0, 12
	s_sub_i32 s6, s7, s0
	s_mul_hi_i32 s0, s7, 0xd5555555
	s_lshr_b32 s1, s0, 31
	s_ashr_i32 s0, s0, 1
	v_mov_b32_e32 v6, v0
	s_add_i32 s28, s0, s1
	s_add_i32 s28, s28, 31
	v_readfirstlane_b32 s0, v6
	s_ashr_i32 s26, s0, 6
	s_lshl_b32 s0, s28, 8
	s_lshl_b32 s27, s26, 5
	v_and_b32_e32 v72, 31, v6
	s_add_i32 s0, s27, s0
	v_bfe_u32 v5, v6, 5, 1
	s_cmp_eq_u32 s28, 0
	v_or_b32_e32 v4, s0, v72
	s_cbranch_scc1 .LBB0_494
	s_lshl_b32 s29, s28, 7
	s_mov_b64 s[0:1], exec
	s_mov_b64 s[10:11], exec
	s_ashr_i32 s7, s6, 31
	s_lshl_b64 s[8:9], s[6:7], 14
	v_readlane_b32 s12, v250, 32
	v_readlane_b32 s13, v250, 33
	v_lshlrev_b32_e32 v7, 2, v6
	s_nop 1
	s_add_u32 s12, s12, s8
	s_addc_u32 s13, s13, s9
	v_cmp_gt_i32_e32 vcc, s29, v6
	s_and_b64 exec, s[10:11], vcc
	s_nop 0
	global_load_dword v10, v7, s[12:13]
	v_add_u32_e32 v2, 0x200, v6
	v_cmp_gt_i32_e32 vcc, s29, v2
	s_and_b64 exec, s[10:11], vcc
	s_nop 0
	global_load_dword v11, v7, s[12:13] offset:2048
	s_add_u32 s12, s12, 0x1000
	s_addc_u32 s13, s13, 0
	v_add_u32_e32 v2, 0x400, v6
	v_cmp_gt_i32_e32 vcc, s29, v2
	s_and_b64 exec, s[10:11], vcc
	s_nop 0
	global_load_dword v12, v7, s[12:13]
	v_add_u32_e32 v2, 0x600, v6
	v_cmp_gt_i32_e32 vcc, s29, v2
	s_and_b64 exec, s[10:11], vcc
	s_nop 0
	global_load_dword v13, v7, s[12:13] offset:2048
	s_add_u32 s12, s12, 0x1000
	s_addc_u32 s13, s13, 0
	v_add_u32_e32 v2, 0x800, v6
	v_cmp_gt_i32_e32 vcc, s29, v2
	s_and_b64 exec, s[10:11], vcc
	s_nop 0
	global_load_dword v14, v7, s[12:13]
	v_add_u32_e32 v2, 0xa00, v6
	v_cmp_gt_i32_e32 vcc, s29, v2
	s_and_b64 exec, s[10:11], vcc
	s_nop 0
	global_load_dword v15, v7, s[12:13] offset:2048
	s_add_u32 s12, s12, 0x1000
	s_addc_u32 s13, s13, 0
	v_add_u32_e32 v2, 0xc00, v6
	v_cmp_gt_i32_e32 vcc, s29, v2
	s_and_b64 exec, s[10:11], vcc
	s_nop 0
	global_load_dword v16, v7, s[12:13]
	v_add_u32_e32 v2, 0xe00, v6
	v_cmp_gt_i32_e32 vcc, s29, v2
	s_and_b64 exec, s[10:11], vcc
	s_nop 0
	global_load_dword v17, v7, s[12:13] offset:2048
	s_mov_b64 exec, s[10:11]
.LBB0_484:
	s_or_b64 exec, exec, s[0:1]
	v_mov_b64_e32 v[8:9], s[80:81]
	v_mad_i64_i32 v[8:9], s[0:1], v4, s20, v[8:9]
	s_lshl_b32 s0, s6, 7
	s_ashr_i32 s1, s0, 31
	v_lshl_add_u64 v[8:9], s[0:1], 1, v[8:9]
	v_lshlrev_b32_e32 v2, 4, v5
	v_lshl_add_u64 v[8:9], v[8:9], 0, v[2:3]
	global_load_dwordx4 v[20:23], v[8:9], off offset:32
	global_load_dwordx4 v[24:27], v[8:9], off
	global_load_dwordx4 v[36:39], v[8:9], off offset:96
	global_load_dwordx4 v[40:43], v[8:9], off offset:64
	global_load_dwordx4 v[52:55], v[8:9], off offset:160
	global_load_dwordx4 v[56:59], v[8:9], off offset:128
	global_load_dwordx4 v[68:71], v[8:9], off offset:224
	global_load_dwordx4 v[74:77], v[8:9], off offset:192
	s_waitcnt vmcnt(8)
	v_readlane_b32 s7, v249, 53
	s_nop 3
	v_lshl_add_u32 v73, v6, 2, s7
	v_cmp_gt_i32_e32 vcc, s29, v6
	s_and_b64 exec, s[10:11], vcc
	ds_write_b32 v73, v10
	v_add_u32_e32 v7, 0x200, v6
	v_cmp_gt_i32_e32 vcc, s29, v7
	s_and_b64 exec, s[10:11], vcc
	ds_write_b32 v73, v11 offset:2048
	v_add_u32_e32 v7, 0x400, v6
	v_cmp_gt_i32_e32 vcc, s29, v7
	s_and_b64 exec, s[10:11], vcc
	ds_write_b32 v73, v12 offset:4096
	v_add_u32_e32 v7, 0x600, v6
	v_cmp_gt_i32_e32 vcc, s29, v7
	s_and_b64 exec, s[10:11], vcc
	ds_write_b32 v73, v13 offset:6144
	v_add_u32_e32 v7, 0x800, v6
	v_cmp_gt_i32_e32 vcc, s29, v7
	s_and_b64 exec, s[10:11], vcc
	ds_write_b32 v73, v14 offset:8192
	v_add_u32_e32 v7, 0xa00, v6
	v_cmp_gt_i32_e32 vcc, s29, v7
	s_and_b64 exec, s[10:11], vcc
	ds_write_b32 v73, v15 offset:10240
	v_add_u32_e32 v7, 0xc00, v6
	v_cmp_gt_i32_e32 vcc, s29, v7
	s_and_b64 exec, s[10:11], vcc
	ds_write_b32 v73, v16 offset:12288
	v_add_u32_e32 v7, 0xe00, v6
	v_cmp_gt_i32_e32 vcc, s29, v7
	s_and_b64 exec, s[10:11], vcc
	ds_write_b32 v73, v17 offset:14336
	s_mov_b64 exec, s[10:11]
	v_xor_b32_e32 v7, 32, v199
	v_readlane_b32 s0, v249, 53
	s_mov_b32 s7, 0
	v_mov_b32_e32 v73, -1
	v_lshl_add_u32 v2, v5, 5, s0
	v_mov_b32_e32 v78, 0xff800000
	s_waitcnt lgkmcnt(0)
	s_barrier
	s_waitcnt vmcnt(7)
	v_lshlrev_b32_e32 v9, 16, v20
	s_waitcnt vmcnt(6)
	v_lshlrev_b32_e32 v8, 16, v24
	v_and_b32_e32 v10, 0xffff0000, v24
	v_lshlrev_b32_e32 v16, 16, v26
	v_and_b32_e32 v18, 0xffff0000, v26
	s_waitcnt vmcnt(4)
	v_lshlrev_b32_e32 v24, 16, v40
	v_and_b32_e32 v26, 0xffff0000, v40
	v_lshlrev_b32_e32 v32, 16, v42
	v_and_b32_e32 v34, 0xffff0000, v42
	s_waitcnt vmcnt(2)
	v_lshlrev_b32_e32 v40, 16, v56
	v_and_b32_e32 v42, 0xffff0000, v56
	v_lshlrev_b32_e32 v48, 16, v58
	v_and_b32_e32 v50, 0xffff0000, v58
	s_waitcnt vmcnt(0)
	v_lshlrev_b32_e32 v56, 16, v74
	v_and_b32_e32 v58, 0xffff0000, v74
	v_and_b32_e32 v74, 64, v199
	v_add_u32_e32 v74, 64, v74
	v_cmp_lt_i32_e32 vcc, v7, v74
	v_and_b32_e32 v11, 0xffff0000, v20
	v_lshlrev_b32_e32 v13, 16, v21
	v_cndmask_b32_e32 v7, v199, v7, vcc
	v_lshlrev_b32_e32 v12, 16, v25
	v_and_b32_e32 v15, 0xffff0000, v21
	v_and_b32_e32 v14, 0xffff0000, v25
	v_lshlrev_b32_e32 v17, 16, v22
	v_and_b32_e32 v19, 0xffff0000, v22
	v_lshlrev_b32_e32 v21, 16, v23
	v_lshlrev_b32_e32 v20, 16, v27
	v_and_b32_e32 v23, 0xffff0000, v23
	v_and_b32_e32 v22, 0xffff0000, v27
	v_lshlrev_b32_e32 v25, 16, v36
	v_and_b32_e32 v27, 0xffff0000, v36
	v_lshlrev_b32_e32 v29, 16, v37
	v_lshlrev_b32_e32 v28, 16, v41
	v_and_b32_e32 v31, 0xffff0000, v37
	v_and_b32_e32 v30, 0xffff0000, v41
	v_lshlrev_b32_e32 v33, 16, v38
	v_and_b32_e32 v35, 0xffff0000, v38
	v_lshlrev_b32_e32 v37, 16, v39
	v_lshlrev_b32_e32 v36, 16, v43
	v_and_b32_e32 v39, 0xffff0000, v39
	v_and_b32_e32 v38, 0xffff0000, v43
	v_lshlrev_b32_e32 v41, 16, v52
	v_and_b32_e32 v43, 0xffff0000, v52
	v_lshlrev_b32_e32 v45, 16, v53
	v_lshlrev_b32_e32 v44, 16, v57
	v_and_b32_e32 v47, 0xffff0000, v53
	v_and_b32_e32 v46, 0xffff0000, v57
	v_lshlrev_b32_e32 v49, 16, v54
	v_and_b32_e32 v51, 0xffff0000, v54
	v_lshlrev_b32_e32 v53, 16, v55
	v_lshlrev_b32_e32 v52, 16, v59
	v_and_b32_e32 v55, 0xffff0000, v55
	v_and_b32_e32 v54, 0xffff0000, v59
	v_lshlrev_b32_e32 v57, 16, v68
	v_and_b32_e32 v59, 0xffff0000, v68
	v_lshlrev_b32_e32 v61, 16, v69
	v_lshlrev_b32_e32 v60, 16, v75
	v_and_b32_e32 v63, 0xffff0000, v69
	v_and_b32_e32 v62, 0xffff0000, v75
	v_lshlrev_b32_e32 v65, 16, v70
	v_lshlrev_b32_e32 v64, 16, v76
	v_and_b32_e32 v67, 0xffff0000, v70
	v_and_b32_e32 v66, 0xffff0000, v76
	v_lshlrev_b32_e32 v69, 16, v71
	v_lshlrev_b32_e32 v68, 16, v77
	v_and_b32_e32 v71, 0xffff0000, v71
	v_and_b32_e32 v70, 0xffff0000, v77
	v_lshlrev_b32_e32 v7, 2, v7
	v_mov_b32_e32 v74, 0xff800000
	v_mov_b32_e32 v75, 0xff800000
	v_mov_b32_e32 v76, -1
	v_mov_b32_e32 v77, -1
